# grid barrier: waiters poll the top-level arrival counter (release when TOP >= (gen+1)*nx), TOPGEN bump dropped; on top of mixer rewrite + flat release
# baseline (speedup 1.0000x reference)
.LBB0_80:
	s_or_b64 exec, exec, s[8:9]
	buffer_inv sc1
	v_cvt_f32_u32_e32 v6, v4
	s_waitcnt vmcnt(0)
	v_readfirstlane_b32 s0, v5
	v_sub_u32_e32 v5, 0, v4
	v_rcp_iflag_f32_e32 v6, v6
	v_add_u32_e32 v7, s0, v3
	v_mul_f32_e32 v6, 0x4f7ffffe, v6
	v_cvt_u32_f32_e32 v6, v6
	v_mul_lo_u32 v3, v5, v6
	v_mul_hi_u32 v3, v6, v3
	v_add_u32_e32 v3, v6, v3
	v_mul_hi_u32 v3, v7, v3
	v_mul_lo_u32 v5, v3, v4
	v_sub_u32_e32 v5, v7, v5
	v_add_u32_e32 v6, 1, v3
	v_sub_u32_e32 v8, v5, v4
	v_cmp_ge_u32_e32 vcc, v5, v4
	s_nop 1
	v_cndmask_b32_e32 v3, v3, v6, vcc
	v_cndmask_b32_e32 v5, v5, v8, vcc
	v_add_u32_e32 v6, 1, v3
	v_cmp_ge_u32_e32 vcc, v5, v4
	v_add_u32_e32 v5, 1, v7
	s_nop 0
	v_cndmask_b32_e32 v3, v3, v6, vcc
	v_mul_lo_u32 v6, v4, v3
	v_add_u32_e32 v4, v6, v4
	v_cmp_ne_u32_e32 vcc, v5, v4
	s_and_saveexec_b64 s[0:1], vcc
	s_xor_b64 s[0:1], exec, s[0:1]
	s_cbranch_execz .LBB0_94
	s_waitcnt lgkmcnt(0)
	s_add_u32 s10, s4, 0x3400
	s_addc_u32 s11, s5, 0
	v_add_u32_e32 v6, 1, v3
	v_mul_lo_u32 v6, v6, v2
	global_load_dword v2, v69, s[10:11] sc1
	s_waitcnt vmcnt(0)
	v_cmp_lt_u32_e32 vcc, v2, v6
	s_and_saveexec_b64 s[8:9], vcc
	s_cbranch_execz .LBB0_93
	s_mov_b32 s22, 1
	s_mov_b64 s[12:13], 0
	s_branch .LBB0_84

.LBB0_88:
	global_load_dword v2, v69, s[10:11] sc1
	s_add_i32 s22, s22, 1
	s_mov_b64 s[18:19], -1
	s_waitcnt vmcnt(0)
	v_cmp_ge_u32_e32 vcc, v2, v6
	s_orn2_b64 s[16:17], vcc, exec
	s_branch .LBB0_83

.LBB0_97:
	s_or_b64 exec, exec, s[8:9]
	v_cvt_f32_u32_e32 v5, v2
	s_waitcnt vmcnt(0)
	v_readfirstlane_b32 s1, v4
	v_sub_u32_e32 v4, 0, v2
	s_add_u32 s0, s4, 0x3500
	v_rcp_iflag_f32_e32 v5, v5
	v_add_u32_e32 v3, s1, v3
	v_add_u32_e32 v6, 1, v3
	s_addc_u32 s1, s5, 0
	v_mul_f32_e32 v5, 0x4f7ffffe, v5
	v_cvt_u32_f32_e32 v5, v5
	s_mov_b64 s[10:11], -1
	v_mul_lo_u32 v4, v4, v5
	v_mul_hi_u32 v4, v5, v4
	v_add_u32_e32 v4, v5, v4
	v_mul_hi_u32 v4, v3, v4
	v_mul_lo_u32 v5, v4, v2
	v_sub_u32_e32 v3, v3, v5
	v_add_u32_e32 v7, 1, v4
	v_sub_u32_e32 v5, v3, v2
	v_cmp_ge_u32_e32 vcc, v3, v2
	s_nop 1
	v_cndmask_b32_e32 v4, v4, v7, vcc
	v_cndmask_b32_e32 v3, v3, v5, vcc
	v_add_u32_e32 v5, 1, v4
	v_cmp_ge_u32_e32 vcc, v3, v2
	s_nop 1
	v_cndmask_b32_e32 v4, v4, v5, vcc
	v_mul_lo_u32 v3, v2, v4
	v_add_u32_e32 v2, v3, v2
	v_cmp_ne_u32_e32 vcc, v6, v2
	v_mov_b32_e32 v6, v2
	v_mov_b64_e32 v[2:3], s[0:1]
	s_and_saveexec_b64 s[8:9], vcc
	s_cbranch_execz .LBB0_109
	global_load_dword v2, v69, s[0:1] offset:-256 sc1
	s_mov_b64 s[14:15], 0
	s_waitcnt vmcnt(0)
	v_cmp_lt_u32_e32 vcc, v2, v6
	s_and_saveexec_b64 s[12:13], vcc
	s_cbranch_execz .LBB0_108
	s_add_u32 s10, s4, 0x200
	s_addc_u32 s11, s5, 0
	s_mov_b32 s22, 1
	s_mov_b64 s[4:5], 0
	s_branch .LBB0_101

.LBB0_105:
	global_load_dword v2, v69, s[0:1] offset:-256 sc1
	s_add_i32 s22, s22, 1
	s_mov_b64 s[18:19], -1
	s_waitcnt vmcnt(0)
	v_cmp_ge_u32_e32 vcc, v2, v6
	s_orn2_b64 s[16:17], vcc, exec
	s_branch .LBB0_100

.LBB0_109:
	s_or_b64 exec, exec, s[8:9]
	s_and_saveexec_b64 s[0:1], s[10:11]
	s_cbranch_execz .LBB0_111
.LBB0_111:
	s_or_b64 exec, exec, s[0:1]
	s_mov_b64 s[0:1], exec
	v_mbcnt_lo_u32_b32 v2, s0, 0
	v_mbcnt_hi_u32_b32 v2, s1, v2
	v_cmp_eq_u32_e32 vcc, 0, v2
	s_waitcnt vmcnt(0)
	s_and_saveexec_b64 s[4:5], vcc
	s_cbranch_execz .LBB0_113
	s_bcnt1_i32_b64 s0, s[0:1]
	v_mov_b32_e32 v2, s0

.LBB0_168:
	s_or_b64 exec, exec, s[8:9]
	s_and_saveexec_b64 s[0:1], s[10:11]
	s_cbranch_execz .LBB0_170
.LBB0_170:
	s_or_b64 exec, exec, s[0:1]
	s_mov_b64 s[0:1], exec
	v_mbcnt_lo_u32_b32 v2, s0, 0
	v_mbcnt_hi_u32_b32 v2, s1, v2
	v_cmp_eq_u32_e32 vcc, 0, v2
	s_waitcnt vmcnt(0)
	s_and_saveexec_b64 s[4:5], vcc
	s_cbranch_execz .LBB0_172
	s_bcnt1_i32_b64 s0, s[0:1]
	v_mov_b32_e32 v2, s0

.LBB0_449:
	s_or_b64 exec, exec, s[8:9]
	buffer_inv sc1
	v_cvt_f32_u32_e32 v6, v4
	s_waitcnt vmcnt(0)
	v_readfirstlane_b32 s0, v5
	v_sub_u32_e32 v5, 0, v4
	v_rcp_iflag_f32_e32 v6, v6
	v_add_u32_e32 v7, s0, v3
	v_mul_f32_e32 v6, 0x4f7ffffe, v6
	v_cvt_u32_f32_e32 v6, v6
	v_mul_lo_u32 v3, v5, v6
	v_mul_hi_u32 v3, v6, v3
	v_add_u32_e32 v3, v6, v3
	v_mul_hi_u32 v3, v7, v3
	v_mul_lo_u32 v5, v3, v4
	v_sub_u32_e32 v5, v7, v5
	v_add_u32_e32 v6, 1, v3
	v_cmp_ge_u32_e32 vcc, v5, v4
	s_nop 1
	v_cndmask_b32_e32 v3, v3, v6, vcc
	v_sub_u32_e32 v6, v5, v4
	v_cndmask_b32_e32 v5, v5, v6, vcc
	v_add_u32_e32 v6, 1, v3
	v_cmp_ge_u32_e32 vcc, v5, v4
	v_add_u32_e32 v5, 1, v7
	s_nop 0
	v_cndmask_b32_e32 v3, v3, v6, vcc
	v_mul_lo_u32 v6, v4, v3
	v_add_u32_e32 v4, v6, v4
	v_cmp_ne_u32_e32 vcc, v5, v4
	s_and_saveexec_b64 s[0:1], vcc
	s_xor_b64 s[0:1], exec, s[0:1]
	s_cbranch_execz .LBB0_463
	s_waitcnt lgkmcnt(0)
	s_add_u32 s10, s4, 0x3400
	s_addc_u32 s11, s5, 0
	v_add_u32_e32 v6, 1, v3
	v_mul_lo_u32 v6, v6, v2
	global_load_dword v2, v69, s[10:11] sc1
	s_waitcnt vmcnt(0)
	v_cmp_lt_u32_e32 vcc, v2, v6
	s_and_saveexec_b64 s[8:9], vcc
	s_cbranch_execz .LBB0_462
	s_mov_b32 s22, 1
	s_mov_b64 s[12:13], 0
	s_branch .LBB0_453

.LBB0_466:
	s_or_b64 exec, exec, s[8:9]
	s_waitcnt vmcnt(0)
	v_readfirstlane_b32 s0, v4
	v_cvt_f32_u32_e32 v4, v2
	v_sub_u32_e32 v5, 0, v2
	v_add_u32_e32 v3, s0, v3
	s_add_u32 s0, s4, 0x3500
	v_rcp_iflag_f32_e32 v4, v4
	s_addc_u32 s1, s5, 0
	s_mov_b64 s[10:11], -1
	v_mul_f32_e32 v4, 0x4f7ffffe, v4
	v_cvt_u32_f32_e32 v4, v4
	v_mul_lo_u32 v5, v5, v4
	v_mul_hi_u32 v5, v4, v5
	v_add_u32_e32 v4, v4, v5
	v_mul_hi_u32 v4, v3, v4
	v_mul_lo_u32 v5, v4, v2
	v_sub_u32_e32 v5, v3, v5
	v_cmp_ge_u32_e32 vcc, v5, v2
	v_add_u32_e32 v6, 1, v4
	v_add_u32_e32 v3, 1, v3
	v_cndmask_b32_e32 v4, v4, v6, vcc
	v_sub_u32_e32 v6, v5, v2
	v_cndmask_b32_e32 v5, v5, v6, vcc
	v_cmp_ge_u32_e32 vcc, v5, v2
	v_add_u32_e32 v5, 1, v4
	s_nop 0
	v_cndmask_b32_e32 v4, v4, v5, vcc
	v_mul_lo_u32 v5, v2, v4
	v_add_u32_e32 v2, v5, v2
	v_cmp_ne_u32_e32 vcc, v3, v2
	v_mov_b32_e32 v6, v2
	v_mov_b64_e32 v[2:3], s[0:1]
	s_and_saveexec_b64 s[8:9], vcc
	s_cbranch_execz .LBB0_478
	global_load_dword v2, v69, s[0:1] offset:-256 sc1
	s_mov_b64 s[14:15], 0
	s_waitcnt vmcnt(0)
	v_cmp_lt_u32_e32 vcc, v2, v6
	s_and_saveexec_b64 s[12:13], vcc
	s_cbranch_execz .LBB0_477
	s_add_u32 s10, s4, 0x200
	s_addc_u32 s11, s5, 0
	s_mov_b32 s22, 1
	s_mov_b64 s[4:5], 0
	s_branch .LBB0_470

.LBB0_478:
	s_or_b64 exec, exec, s[8:9]
	s_and_saveexec_b64 s[0:1], s[10:11]
	s_cbranch_execz .LBB0_480
.LBB0_480:
	s_or_b64 exec, exec, s[0:1]
	s_mov_b64 s[0:1], exec
	v_mbcnt_lo_u32_b32 v2, s0, 0
	v_mbcnt_hi_u32_b32 v2, s1, v2
	v_cmp_eq_u32_e32 vcc, 0, v2
	s_waitcnt vmcnt(0)
	s_and_saveexec_b64 s[4:5], vcc
	s_cbranch_execz .LBB0_482
	s_bcnt1_i32_b64 s0, s[0:1]
	v_mov_b32_e32 v2, s0

.LBB0_581:
	s_or_b64 exec, exec, s[8:9]
	s_and_saveexec_b64 s[0:1], s[10:11]
	s_cbranch_execz .LBB0_583
.LBB0_583:
	s_or_b64 exec, exec, s[0:1]
	s_mov_b64 s[0:1], exec
	v_mbcnt_lo_u32_b32 v2, s0, 0
	v_mbcnt_hi_u32_b32 v2, s1, v2
	v_cmp_eq_u32_e32 vcc, 0, v2
	s_waitcnt vmcnt(0)
	s_and_saveexec_b64 s[4:5], vcc
	s_cbranch_execz .LBB0_585
	s_bcnt1_i32_b64 s0, s[0:1]
	v_mov_b32_e32 v2, s0

.LBB0_638:
	s_or_b64 exec, exec, s[8:9]
	s_and_saveexec_b64 s[0:1], s[10:11]
	s_cbranch_execz .LBB0_640
.LBB0_640:
	s_or_b64 exec, exec, s[0:1]
	s_mov_b64 s[0:1], exec
	v_mbcnt_lo_u32_b32 v2, s0, 0
	v_mbcnt_hi_u32_b32 v2, s1, v2
	v_cmp_eq_u32_e32 vcc, 0, v2
	s_waitcnt vmcnt(0)
	s_and_saveexec_b64 s[4:5], vcc
	s_cbranch_execz .LBB0_642
	s_bcnt1_i32_b64 s0, s[0:1]
	v_mov_b32_e32 v2, s0

.LBB0_756:
	s_or_b64 exec, exec, s[8:9]
	s_and_saveexec_b64 s[0:1], s[10:11]
	s_cbranch_execz .LBB0_758
.LBB0_758:
	s_or_b64 exec, exec, s[0:1]
	s_mov_b64 s[0:1], exec
	v_mbcnt_lo_u32_b32 v2, s0, 0
	v_mbcnt_hi_u32_b32 v2, s1, v2
	v_cmp_eq_u32_e32 vcc, 0, v2
	s_waitcnt vmcnt(0)
	s_and_saveexec_b64 s[4:5], vcc
	s_cbranch_execz .LBB0_760
	s_bcnt1_i32_b64 s0, s[0:1]
	v_mov_b32_e32 v2, s0

.LBB0_869:
	s_or_b64 exec, exec, s[8:9]
	s_and_saveexec_b64 s[0:1], s[10:11]
	s_cbranch_execz .LBB0_871
.LBB0_871:
	s_or_b64 exec, exec, s[0:1]
	s_mov_b64 s[0:1], exec
	v_mbcnt_lo_u32_b32 v2, s0, 0
	v_mbcnt_hi_u32_b32 v2, s1, v2
	v_cmp_eq_u32_e32 vcc, 0, v2
	s_waitcnt vmcnt(0)
	s_and_saveexec_b64 s[4:5], vcc
	s_cbranch_execz .LBB0_873
	s_bcnt1_i32_b64 s0, s[0:1]
	v_mov_b32_e32 v2, s0

.LBB0_940:
	s_or_b64 exec, exec, s[8:9]
	s_and_saveexec_b64 s[0:1], s[10:11]
	s_cbranch_execz .LBB0_942
.LBB0_942:
	s_or_b64 exec, exec, s[0:1]
	s_mov_b64 s[0:1], exec
	v_mbcnt_lo_u32_b32 v2, s0, 0
	v_mbcnt_hi_u32_b32 v2, s1, v2
	v_cmp_eq_u32_e32 vcc, 0, v2
	s_waitcnt vmcnt(0)
	s_and_saveexec_b64 s[4:5], vcc
	s_cbranch_execz .LBB0_944
	s_bcnt1_i32_b64 s0, s[0:1]
	v_mov_b32_e32 v2, s0

.LBB0_1009:
	s_or_b64 exec, exec, s[8:9]
	s_and_saveexec_b64 s[0:1], s[10:11]
	s_cbranch_execz .LBB0_1011
.LBB0_1011:
	s_or_b64 exec, exec, s[0:1]
	s_mov_b64 s[0:1], exec
	v_mbcnt_lo_u32_b32 v2, s0, 0
	v_mbcnt_hi_u32_b32 v2, s1, v2
	v_cmp_eq_u32_e32 vcc, 0, v2
	s_waitcnt vmcnt(0)
	s_and_saveexec_b64 s[4:5], vcc
	s_cbranch_execz .LBB0_1013
	s_bcnt1_i32_b64 s0, s[0:1]
	v_mov_b32_e32 v2, s0

.LBB0_1155:
	s_or_b64 exec, exec, s[8:9]
	s_and_saveexec_b64 s[0:1], s[10:11]
	s_cbranch_execz .LBB0_1157
.LBB0_1157:
	s_or_b64 exec, exec, s[0:1]
	s_mov_b64 s[0:1], exec
	v_mbcnt_lo_u32_b32 v2, s0, 0
	v_mbcnt_hi_u32_b32 v2, s1, v2
	v_cmp_eq_u32_e32 vcc, 0, v2
	s_waitcnt vmcnt(0)
	s_and_saveexec_b64 s[4:5], vcc
	s_cbranch_execz .LBB0_1159
	s_bcnt1_i32_b64 s0, s[0:1]
	v_mov_b32_e32 v2, s0

.LBB0_1293:
	s_or_b64 exec, exec, s[8:9]
	s_and_saveexec_b64 s[0:1], s[10:11]
	s_cbranch_execz .LBB0_1295
.LBB0_1295:
	s_or_b64 exec, exec, s[0:1]
	s_mov_b64 s[0:1], exec
	v_mbcnt_lo_u32_b32 v2, s0, 0
	v_mbcnt_hi_u32_b32 v2, s1, v2
	v_cmp_eq_u32_e32 vcc, 0, v2
	s_waitcnt vmcnt(0)
	s_and_saveexec_b64 s[4:5], vcc
	s_cbranch_execz .LBB0_1297
	s_bcnt1_i32_b64 s0, s[0:1]
	v_mov_b32_e32 v2, s0

.LBB0_1483:
	s_or_b64 exec, exec, s[8:9]
	v_cvt_f32_u32_e32 v6, v4
	s_waitcnt vmcnt(0)
	v_readfirstlane_b32 s0, v5
	v_sub_u32_e32 v5, 0, v4
	v_rcp_iflag_f32_e32 v6, v6
	v_add_u32_e32 v7, s0, v3
	v_mul_f32_e32 v6, 0x4f7ffffe, v6
	v_cvt_u32_f32_e32 v6, v6
	v_mul_lo_u32 v3, v5, v6
	v_mul_hi_u32 v3, v6, v3
	v_add_u32_e32 v3, v6, v3
	v_mul_hi_u32 v3, v7, v3
	v_mul_lo_u32 v5, v3, v4
	v_sub_u32_e32 v5, v7, v5
	v_add_u32_e32 v6, 1, v3
	v_cmp_ge_u32_e32 vcc, v5, v4
	s_nop 1
	v_cndmask_b32_e32 v3, v3, v6, vcc
	v_sub_u32_e32 v6, v5, v4
	v_cndmask_b32_e32 v5, v5, v6, vcc
	v_add_u32_e32 v6, 1, v3
	v_cmp_ge_u32_e32 vcc, v5, v4
	v_add_u32_e32 v5, 1, v7
	s_nop 0
	v_cndmask_b32_e32 v3, v3, v6, vcc
	v_mul_lo_u32 v6, v4, v3
	v_add_u32_e32 v4, v6, v4
	v_cmp_ne_u32_e32 vcc, v5, v4
	s_and_saveexec_b64 s[0:1], vcc
	s_xor_b64 s[0:1], exec, s[0:1]
	s_cbranch_execz .LBB0_1497
	s_waitcnt lgkmcnt(0)
	s_add_u32 s10, s4, 0x3400
	s_addc_u32 s11, s5, 0
	v_add_u32_e32 v6, 1, v3
	v_mul_lo_u32 v6, v6, v2
	global_load_dword v2, v69, s[10:11] sc1
	s_waitcnt vmcnt(0)
	v_cmp_lt_u32_e32 vcc, v2, v6
	s_and_saveexec_b64 s[8:9], vcc
	s_cbranch_execz .LBB0_1496
	s_mov_b32 s22, 1
	s_mov_b64 s[12:13], 0
	s_branch .LBB0_1487

.LBB0_1512:
	s_or_b64 exec, exec, s[8:9]
	s_and_saveexec_b64 s[0:1], s[10:11]
	s_cbranch_execz .LBB0_1514
.LBB0_1514:
	s_or_b64 exec, exec, s[0:1]
	s_mov_b64 s[0:1], exec
	v_mbcnt_lo_u32_b32 v2, s0, 0
	v_mbcnt_hi_u32_b32 v2, s1, v2
	v_cmp_eq_u32_e32 vcc, 0, v2
	s_waitcnt vmcnt(0)
	buffer_inv sc1
	s_and_saveexec_b64 s[4:5], vcc
	s_cbranch_execz .LBB0_1516
	s_bcnt1_i32_b64 s0, s[0:1]
	v_mov_b32_e32 v2, s0

.LBB0_1667:
	s_or_b64 exec, exec, s[8:9]
	s_and_saveexec_b64 s[0:1], s[10:11]
	s_cbranch_execz .LBB0_1669
.LBB0_1669:
	s_or_b64 exec, exec, s[0:1]
	s_mov_b64 s[0:1], exec
	v_mbcnt_lo_u32_b32 v2, s0, 0
	v_mbcnt_hi_u32_b32 v2, s1, v2
	v_cmp_eq_u32_e32 vcc, 0, v2
	s_waitcnt vmcnt(0)
	s_and_saveexec_b64 s[4:5], vcc
	s_cbranch_execz .LBB0_1671
	s_bcnt1_i32_b64 s0, s[0:1]
	v_mov_b32_e32 v2, s0
